# 16 KiB static LDS on top of the dynamic 144 KiB: P5 next-head conv weights and the unit tail's RMSNorm weights read from per-phase LDS copies instead of global loads; tail second batch without vmcnt w
# speedup vs baseline: 1.0063x; 1.0001x over previous
.LBB0_541:
	v_readlane_b32 s0, v253, 12
	v_readlane_b32 s1, v253, 13
	s_mov_b64 s[4:5], s[0:1]
	s_cmp_lt_i32 s4, 6
	v_readlane_b32 s2, v253, 14
	v_readlane_b32 s3, v253, 15
	s_cselect_b64 s[0:1], -1, 0
	s_cmp_gt_i32 s5, 5
	s_cselect_b64 s[2:3], -1, 0
	s_and_b64 s[0:1], s[0:1], s[2:3]
	v_writelane_b32 v253, s0, 53
	s_andn2_b64 vcc, exec, s[0:1]
	s_nop 0
	v_writelane_b32 v253, s1, 54
	s_cbranch_vccnz .LBB0_600
	s_cmpk_gt_i32 s82, 0x3ff
	s_cbranch_scc1 .LBB0_600
	s_mov_b32 s98, 1
	s_cmp_gt_u32 s84, 3
	s_cbranch_scc0 .Lp5_noprio
	s_setprio 2

.LBB0_544:
	v_and_b32_e32 v111, 48, v207
	v_add_u32_e32 v111, 0x26800, v111
	v_readlane_b32 s2, v255, 58
	s_lshl_b32 s0, s2, 2
	s_mov_b32 s1, s3
	v_lshl_add_u64 v[54:55], v[168:169], 0, s[0:1]
	ds_read_b128 v[60:63], v111
	ds_read_b128 v[64:67], v111 offset:64
	ds_read_b128 v[68:71], v111 offset:128
	ds_read_b128 v[72:75], v111 offset:192
	v_add_u32_e32 v6, s50, v232
	v_ashrrev_i32_e32 v7, 31, v6
	ds_read_b128 v[76:79], v159 offset:16384
	ds_read_b128 v[80:83], v159 offset:24576
	ds_read_b128 v[84:87], v159 offset:8192
	ds_read_b128 v[50:53], v159 offset:32768
	ds_read_b128 v[38:41], v214
	ds_read_b128 v[26:29], v214 offset:8192
	ds_read_b128 v[14:17], v214 offset:16384
	ds_read_b128 v[2:5], v214 offset:24576
	v_lshlrev_b64 v[56:57], 13, v[6:7]
	ds_read_b128 v[88:91], v111 offset:256
	ds_read_b128 v[92:95], v111 offset:320
	ds_read_b128 v[96:99], v111 offset:384
	ds_read_b128 v[100:103], v111 offset:448
	ds_read_b128 v[46:49], v111 offset:512
	ds_read_b128 v[42:45], v111 offset:576
	ds_read_b128 v[34:37], v111 offset:640
	ds_read_b128 v[30:33], v111 offset:704
	ds_read_b128 v[22:25], v111 offset:768
	ds_read_b128 v[18:21], v111 offset:832
	ds_read_b128 v[10:13], v111 offset:896
	ds_read_b128 v[6:9], v111 offset:960
	ds_bpermute_b32 v1, v240, v140
	v_readlane_b32 s0, v253, 57
	v_readlane_b32 s1, v253, 58
	s_waitcnt lgkmcnt(6)
	v_lshlrev_b32_e32 v104, 16, v84
	v_and_b32_e32 v84, 0xffff0000, v84
	s_waitcnt lgkmcnt(0)
	v_add_f32_e32 v1, v140, v1
	ds_bpermute_b32 v107, v241, v1
	v_lshl_add_u64 v[58:59], s[0:1], 0, v[56:57]
	s_mov_b32 s0, 0x800000
	v_lshlrev_b32_e32 v105, 16, v85
	v_and_b32_e32 v85, 0xffff0000, v85
	s_waitcnt lgkmcnt(0)
	v_add_f32_e32 v1, v1, v107
	v_fmamk_f32 v1, v1, 0x3b000000, v250
	v_mul_f32_e32 v107, 0x4b800000, v1
	v_cmp_gt_f32_e32 vcc, s0, v1
	v_mov_b32_e32 v173, v161
	v_lshlrev_b32_e32 v106, 16, v86
	v_cndmask_b32_e32 v1, v1, v107, vcc
	v_rsq_f32_e32 v1, v1
	v_and_b32_e32 v86, 0xffff0000, v86
	v_lshlrev_b32_e32 v108, 16, v87
	v_and_b32_e32 v87, 0xffff0000, v87
	v_mul_f32_e32 v110, 0x45800000, v1
	v_cndmask_b32_e32 v1, v1, v110, vcc
	v_mul_f32_e32 v104, v1, v104
	v_mul_f32_e32 v84, v1, v84
	v_mul_f32_e32 v105, v1, v105
	v_mul_f32_e32 v85, v1, v85
	s_lshl_b32 s2, s2, 1
	v_lshl_add_u64 v[56:57], v[58:59], 0, v[172:173]
	v_mul_f32_e32 v106, v1, v106
	v_mul_f32_e32 v86, v1, v86
	v_mul_f32_e32 v108, v1, v108
	v_mul_f32_e32 v87, v1, v87
	v_lshl_add_u64 v[56:57], v[56:57], 0, s[2:3]
	s_waitcnt vmcnt(0)
	global_load_dwordx4 v[112:115], v[56:57], off offset:512
	global_load_dwordx4 v[116:119], v[56:57], off offset:576
	global_load_dwordx4 v[120:123], v[56:57], off offset:640
	global_load_dwordx4 v[124:127], v[56:57], off offset:704
	global_load_dwordx4 v[128:131], v[56:57], off offset:768
	global_load_dwordx4 v[132:135], v[56:57], off offset:832
	global_load_dwordx4 v[136:139], v[56:57], off offset:896
	global_load_dwordx4 v[176:179], v[56:57], off offset:960
	v_lshlrev_b32_e32 v107, 16, v76
	v_and_b32_e32 v76, 0xffff0000, v76
	v_lshlrev_b32_e32 v109, 16, v77
	v_mul_f32_e32 v107, v1, v107
	v_mul_f32_e32 v76, v1, v76
	v_mul_f32_e32 v109, v1, v109
	v_readlane_b32 s83, v255, 57
	v_readlane_b32 s0, v255, 55
	s_add_i32 s49, s49, s83
	s_add_i32 s0, s0, s83
	v_writelane_b32 v255, s0, 55
	s_cmpk_lt_i32 s49, 0x400
	s_mov_b32 s84, s53
	s_mov_b64 s[86:87], s[54:55]
	s_mov_b32 s85, 0x41a00000
	s_waitcnt vmcnt(8)
	v_mul_f32_e32 v60, v60, v104
	v_mul_f32_e32 v61, v61, v84
	v_mul_f32_e32 v62, v62, v105
	v_mul_f32_e32 v63, v63, v85
	s_waitcnt vmcnt(8)
	v_mul_f32_e32 v64, v64, v106
	v_mul_f32_e32 v65, v65, v86
	v_mul_f32_e32 v66, v66, v108
	v_mul_f32_e32 v67, v67, v87
	v_cvt_pk_bf16_f32 v60, v60, v61
	v_cvt_pk_bf16_f32 v61, v62, v63
	v_cvt_pk_bf16_f32 v62, v64, v65
	v_cvt_pk_bf16_f32 v63, v66, v67
	global_store_dwordx4 v[56:57], v[60:63], off
	s_waitcnt vmcnt(9)
	v_mul_f32_e32 v68, v68, v107
	v_mul_f32_e32 v69, v69, v76
	v_and_b32_e32 v61, 0xffff0000, v77
	v_lshlrev_b32_e32 v62, 16, v78
	v_and_b32_e32 v63, 0xffff0000, v78
	v_mul_f32_e32 v61, v1, v61
	v_mul_f32_e32 v62, v1, v62
	v_mul_f32_e32 v63, v1, v63
	v_mul_f32_e32 v61, v71, v61
	s_waitcnt vmcnt(9)
	v_mul_f32_e32 v62, v72, v62
	v_mul_f32_e32 v63, v73, v63
	v_mul_f32_e32 v70, v70, v109
	v_cvt_pk_bf16_f32 v60, v68, v69
	v_cvt_pk_bf16_f32 v61, v70, v61
	v_cvt_pk_bf16_f32 v62, v62, v63
	v_lshlrev_b32_e32 v63, 16, v79
	v_mul_f32_e32 v63, v1, v63
	v_and_b32_e32 v64, 0xffff0000, v79
	v_mul_f32_e32 v63, v74, v63
	v_mul_f32_e32 v64, v1, v64
	v_mul_f32_e32 v64, v75, v64
	v_cvt_pk_bf16_f32 v63, v63, v64
	global_store_dwordx4 v[56:57], v[60:63], off offset:64
	v_and_b32_e32 v64, 0xffff0000, v83
	v_mul_f32_e32 v64, v1, v64
	v_lshlrev_b32_e32 v60, 16, v80
	v_and_b32_e32 v61, 0xffff0000, v80
	v_mul_f32_e32 v60, v1, v60
	v_mul_f32_e32 v61, v1, v61
	s_waitcnt vmcnt(10)
	v_mul_f32_e32 v60, v88, v60
	v_mul_f32_e32 v61, v89, v61
	v_cvt_pk_bf16_f32 v60, v60, v61
	v_lshlrev_b32_e32 v61, 16, v81
	v_and_b32_e32 v62, 0xffff0000, v81
	v_mul_f32_e32 v61, v1, v61
	v_mul_f32_e32 v62, v1, v62
	v_mul_f32_e32 v61, v90, v61
	v_mul_f32_e32 v62, v91, v62
	v_cvt_pk_bf16_f32 v61, v61, v62
	v_lshlrev_b32_e32 v62, 16, v82
	v_and_b32_e32 v63, 0xffff0000, v82
	v_mul_f32_e32 v62, v1, v62
	v_mul_f32_e32 v63, v1, v63
	s_waitcnt vmcnt(10)
	v_mul_f32_e32 v62, v92, v62
	v_mul_f32_e32 v63, v93, v63
	v_cvt_pk_bf16_f32 v62, v62, v63
	v_lshlrev_b32_e32 v63, 16, v83
	v_mul_f32_e32 v63, v1, v63
	v_mul_f32_e32 v63, v94, v63
	v_mul_f32_e32 v64, v95, v64
	v_cvt_pk_bf16_f32 v63, v63, v64
	global_store_dwordx4 v[56:57], v[60:63], off offset:128
	s_nop 1
	v_lshlrev_b32_e32 v60, 16, v50
	v_and_b32_e32 v50, 0xffff0000, v50
	v_mul_f32_e32 v60, v1, v60
	v_mul_f32_e32 v50, v1, v50
	s_waitcnt vmcnt(11)
	v_mul_f32_e32 v60, v96, v60
	v_mul_f32_e32 v50, v97, v50
	v_cvt_pk_bf16_f32 v50, v60, v50
	v_lshlrev_b32_e32 v60, 16, v51
	v_and_b32_e32 v51, 0xffff0000, v51
	v_mul_f32_e32 v60, v1, v60
	v_mul_f32_e32 v51, v1, v51
	v_mul_f32_e32 v60, v98, v60
	v_mul_f32_e32 v51, v99, v51
	v_cvt_pk_bf16_f32 v51, v60, v51
	v_lshlrev_b32_e32 v60, 16, v52
	v_and_b32_e32 v52, 0xffff0000, v52
	v_mul_f32_e32 v60, v1, v60
	v_mul_f32_e32 v52, v1, v52
	s_waitcnt vmcnt(11)
	v_mul_f32_e32 v60, v100, v60
	v_mul_f32_e32 v52, v101, v52
	v_cvt_pk_bf16_f32 v52, v60, v52
	v_lshlrev_b32_e32 v60, 16, v53
	v_and_b32_e32 v53, 0xffff0000, v53
	v_mul_f32_e32 v53, v1, v53
	v_mul_f32_e32 v60, v1, v60
	v_mul_f32_e32 v53, v103, v53
	v_mul_f32_e32 v60, v102, v60
	v_cvt_pk_bf16_f32 v53, v60, v53
	global_store_dwordx4 v[56:57], v[50:53], off offset:192
	s_nop 1
	v_lshlrev_b32_e32 v50, 16, v38
	v_and_b32_e32 v38, 0xffff0000, v38
	v_mul_f32_e32 v50, v1, v50
	v_mul_f32_e32 v38, v1, v38
	s_waitcnt vmcnt(12)
	v_mul_f32_e32 v46, v46, v50
	v_mul_f32_e32 v38, v47, v38
	v_cvt_pk_bf16_f32 v38, v46, v38
	v_lshlrev_b32_e32 v46, 16, v39
	v_and_b32_e32 v39, 0xffff0000, v39
	v_mul_f32_e32 v46, v1, v46
	v_mul_f32_e32 v39, v1, v39
	v_mul_f32_e32 v46, v48, v46
	v_mul_f32_e32 v39, v49, v39
	v_cvt_pk_bf16_f32 v39, v46, v39
	v_lshlrev_b32_e32 v46, 16, v40
	v_and_b32_e32 v40, 0xffff0000, v40
	v_mul_f32_e32 v46, v1, v46
	v_mul_f32_e32 v40, v1, v40
	s_waitcnt vmcnt(12)
	v_mul_f32_e32 v42, v42, v46
	v_mul_f32_e32 v40, v43, v40
	v_cvt_pk_bf16_f32 v40, v42, v40
	v_lshlrev_b32_e32 v42, 16, v41
	v_and_b32_e32 v41, 0xffff0000, v41
	v_mul_f32_e32 v41, v1, v41
	v_mul_f32_e32 v42, v1, v42
	v_mul_f32_e32 v41, v45, v41
	v_mul_f32_e32 v42, v44, v42
	v_cvt_pk_bf16_f32 v41, v42, v41
	global_store_dwordx4 v[56:57], v[38:41], off offset:256
	s_nop 1
	v_lshlrev_b32_e32 v38, 16, v26
	v_and_b32_e32 v26, 0xffff0000, v26
	v_mul_f32_e32 v38, v1, v38
	v_mul_f32_e32 v26, v1, v26
	s_waitcnt vmcnt(13)
	v_mul_f32_e32 v34, v34, v38
	v_mul_f32_e32 v26, v35, v26
	v_cvt_pk_bf16_f32 v26, v34, v26
	v_lshlrev_b32_e32 v34, 16, v27
	v_and_b32_e32 v27, 0xffff0000, v27
	v_mul_f32_e32 v34, v1, v34
	v_mul_f32_e32 v27, v1, v27
	v_mul_f32_e32 v34, v36, v34
	v_mul_f32_e32 v27, v37, v27
	v_cvt_pk_bf16_f32 v27, v34, v27
	v_lshlrev_b32_e32 v34, 16, v28
	v_and_b32_e32 v28, 0xffff0000, v28
	v_mul_f32_e32 v34, v1, v34
	v_mul_f32_e32 v28, v1, v28
	s_waitcnt vmcnt(13)
	v_mul_f32_e32 v30, v30, v34
	v_mul_f32_e32 v28, v31, v28
	v_cvt_pk_bf16_f32 v28, v30, v28
	v_lshlrev_b32_e32 v30, 16, v29
	v_and_b32_e32 v29, 0xffff0000, v29
	v_mul_f32_e32 v29, v1, v29
	v_mul_f32_e32 v30, v1, v30
	v_mul_f32_e32 v29, v33, v29
	v_mul_f32_e32 v30, v32, v30
	v_cvt_pk_bf16_f32 v29, v30, v29
	global_store_dwordx4 v[56:57], v[26:29], off offset:320
	s_nop 1
	v_lshlrev_b32_e32 v26, 16, v14
	v_and_b32_e32 v14, 0xffff0000, v14
	v_mul_f32_e32 v26, v1, v26
	v_mul_f32_e32 v14, v1, v14
	s_waitcnt vmcnt(14)
	v_mul_f32_e32 v22, v22, v26
	v_mul_f32_e32 v14, v23, v14
	v_cvt_pk_bf16_f32 v14, v22, v14
	v_lshlrev_b32_e32 v22, 16, v15
	v_and_b32_e32 v15, 0xffff0000, v15
	v_mul_f32_e32 v22, v1, v22
	v_mul_f32_e32 v15, v1, v15
	v_mul_f32_e32 v22, v24, v22
	v_mul_f32_e32 v15, v25, v15
	v_cvt_pk_bf16_f32 v15, v22, v15
	v_lshlrev_b32_e32 v22, 16, v16
	v_and_b32_e32 v16, 0xffff0000, v16
	v_mul_f32_e32 v22, v1, v22
	v_mul_f32_e32 v16, v1, v16
	s_waitcnt vmcnt(14)
	v_mul_f32_e32 v18, v18, v22
	v_mul_f32_e32 v16, v19, v16
	v_cvt_pk_bf16_f32 v16, v18, v16
	v_lshlrev_b32_e32 v18, 16, v17
	v_and_b32_e32 v17, 0xffff0000, v17
	v_mul_f32_e32 v17, v1, v17
	v_mul_f32_e32 v18, v1, v18
	v_mul_f32_e32 v17, v21, v17
	v_mul_f32_e32 v18, v20, v18
	v_cvt_pk_bf16_f32 v17, v18, v17
	global_store_dwordx4 v[56:57], v[14:17], off offset:384
	s_nop 1
	v_lshlrev_b32_e32 v14, 16, v2
	v_and_b32_e32 v2, 0xffff0000, v2
	v_mul_f32_e32 v14, v1, v14
	v_mul_f32_e32 v2, v1, v2
	s_waitcnt vmcnt(15)
	v_mul_f32_e32 v10, v10, v14
	v_mul_f32_e32 v2, v11, v2
	v_cvt_pk_bf16_f32 v2, v10, v2
	v_lshlrev_b32_e32 v10, 16, v3
	v_and_b32_e32 v3, 0xffff0000, v3
	v_mul_f32_e32 v10, v1, v10
	v_mul_f32_e32 v3, v1, v3
	v_mul_f32_e32 v10, v12, v10
	v_mul_f32_e32 v3, v13, v3
	v_cvt_pk_bf16_f32 v3, v10, v3
	v_lshlrev_b32_e32 v10, 16, v4
	v_and_b32_e32 v4, 0xffff0000, v4
	v_mul_f32_e32 v10, v1, v10
	v_mul_f32_e32 v4, v1, v4
	s_waitcnt vmcnt(15)
	v_mul_f32_e32 v6, v6, v10
	v_mul_f32_e32 v4, v7, v4
	v_cvt_pk_bf16_f32 v4, v6, v4
	v_lshlrev_b32_e32 v6, 16, v5
	v_and_b32_e32 v5, 0xffff0000, v5
	v_mul_f32_e32 v5, v1, v5
	v_mul_f32_e32 v6, v1, v6
	v_mul_f32_e32 v5, v9, v5
	v_mul_f32_e32 v6, v8, v6
	v_cvt_pk_bf16_f32 v5, v6, v5
	global_store_dwordx4 v[56:57], v[2:5], off offset:448
	s_waitcnt vmcnt(8)
	v_mov_b64_e32 v[12:13], v[112:113]
	v_mov_b64_e32 v[14:15], v[114:115]
	ds_read_b128 v[16:19], v111 offset:1024
	ds_read_b128 v[20:23], v111 offset:1088
	v_mov_b64_e32 v[24:25], v[116:117]
	v_mov_b64_e32 v[26:27], v[118:119]
	ds_read_b128 v[28:31], v111 offset:1152
	ds_read_b128 v[32:35], v111 offset:1216
	v_mov_b64_e32 v[36:37], v[120:121]
	v_mov_b64_e32 v[38:39], v[122:123]
	ds_read_b128 v[40:43], v111 offset:1280
	v_lshl_add_u64 v[2:3], v[58:59], 0, s[2:3]
	v_lshl_add_u64 v[10:11], v[2:3], 0, v[172:173]
	ds_read_b128 v[44:47], v111 offset:1344
	ds_read_b128 v[48:51], v111 offset:1408
	ds_read_b128 v[58:61], v111 offset:1472
	v_mov_b64_e32 v[62:63], v[124:125]
	v_mov_b64_e32 v[64:65], v[126:127]
	ds_read_b128 v[66:69], v111 offset:1536
	ds_read_b128 v[70:73], v111 offset:1600
	ds_read_b128 v[74:77], v111 offset:1664
	ds_read_b128 v[78:81], v111 offset:1728
	v_mov_b64_e32 v[82:83], v[128:129]
	v_mov_b64_e32 v[84:85], v[130:131]
	v_mov_b64_e32 v[86:87], v[132:133]
	v_mov_b64_e32 v[88:89], v[134:135]
	ds_read_b128 v[90:93], v111 offset:1792
	ds_read_b128 v[94:97], v111 offset:1856
	ds_read_b128 v[98:101], v111 offset:1920
	ds_read_b128 v[2:5], v111 offset:1984
	s_nop 0
	v_mov_b64_e32 v[52:53], v[136:137]
	v_mov_b64_e32 v[54:55], v[138:139]
	v_mov_b64_e32 v[6:7], v[176:177]
	v_mov_b64_e32 v[8:9], v[178:179]
	s_waitcnt lgkmcnt(0)
	s_nop 0
	v_lshlrev_b32_e32 v56, 16, v12
	v_and_b32_e32 v12, 0xffff0000, v12
	v_mul_f32_e32 v56, v1, v56
	v_mul_f32_e32 v12, v1, v12
	s_nop 0
	v_mul_f32_e32 v16, v16, v56
	v_mul_f32_e32 v12, v17, v12
	v_cvt_pk_bf16_f32 v12, v16, v12
	v_lshlrev_b32_e32 v16, 16, v13
	v_and_b32_e32 v13, 0xffff0000, v13
	v_mul_f32_e32 v16, v1, v16
	v_mul_f32_e32 v13, v1, v13
	v_mul_f32_e32 v16, v18, v16
	v_mul_f32_e32 v13, v19, v13
	v_cvt_pk_bf16_f32 v13, v16, v13
	v_lshlrev_b32_e32 v16, 16, v14
	v_and_b32_e32 v14, 0xffff0000, v14
	v_mul_f32_e32 v16, v1, v16
	v_mul_f32_e32 v14, v1, v14
	s_nop 0
	v_mul_f32_e32 v16, v20, v16
	v_mul_f32_e32 v14, v21, v14
	v_cvt_pk_bf16_f32 v14, v16, v14
	v_lshlrev_b32_e32 v16, 16, v15
	v_and_b32_e32 v15, 0xffff0000, v15
	v_mul_f32_e32 v15, v1, v15
	v_mul_f32_e32 v16, v1, v16
	v_mul_f32_e32 v15, v23, v15
	v_mul_f32_e32 v16, v22, v16
	v_cvt_pk_bf16_f32 v15, v16, v15
	global_store_dwordx4 v[10:11], v[12:15], off offset:512
	s_nop 0
	v_and_b32_e32 v16, 0xffff0000, v27
	v_mul_f32_e32 v16, v1, v16
	v_lshlrev_b32_e32 v12, 16, v24
	v_and_b32_e32 v13, 0xffff0000, v24
	v_mul_f32_e32 v12, v1, v12
	v_mul_f32_e32 v13, v1, v13
	s_nop 0
	v_mul_f32_e32 v12, v28, v12
	v_mul_f32_e32 v13, v29, v13
	v_cvt_pk_bf16_f32 v12, v12, v13
	v_lshlrev_b32_e32 v13, 16, v25
	v_and_b32_e32 v14, 0xffff0000, v25
	v_mul_f32_e32 v13, v1, v13
	v_mul_f32_e32 v14, v1, v14
	v_mul_f32_e32 v13, v30, v13
	v_mul_f32_e32 v14, v31, v14
	v_cvt_pk_bf16_f32 v13, v13, v14
	v_lshlrev_b32_e32 v14, 16, v26
	v_and_b32_e32 v15, 0xffff0000, v26
	v_mul_f32_e32 v14, v1, v14
	v_mul_f32_e32 v15, v1, v15
	s_nop 0
	v_mul_f32_e32 v14, v32, v14
	v_mul_f32_e32 v15, v33, v15
	v_cvt_pk_bf16_f32 v14, v14, v15
	v_lshlrev_b32_e32 v15, 16, v27
	v_mul_f32_e32 v15, v1, v15
	v_mul_f32_e32 v15, v34, v15
	v_mul_f32_e32 v16, v35, v16
	v_cvt_pk_bf16_f32 v15, v15, v16
	global_store_dwordx4 v[10:11], v[12:15], off offset:576
	s_nop 0
	v_and_b32_e32 v16, 0xffff0000, v39
	v_mul_f32_e32 v16, v1, v16
	v_lshlrev_b32_e32 v12, 16, v36
	v_and_b32_e32 v13, 0xffff0000, v36
	v_mul_f32_e32 v12, v1, v12
	v_mul_f32_e32 v13, v1, v13
	s_nop 0
	v_mul_f32_e32 v12, v40, v12
	v_mul_f32_e32 v13, v41, v13
	v_cvt_pk_bf16_f32 v12, v12, v13
	v_lshlrev_b32_e32 v13, 16, v37
	v_and_b32_e32 v14, 0xffff0000, v37
	v_mul_f32_e32 v13, v1, v13
	v_mul_f32_e32 v14, v1, v14
	v_mul_f32_e32 v13, v42, v13
	v_mul_f32_e32 v14, v43, v14
	v_cvt_pk_bf16_f32 v13, v13, v14
	v_lshlrev_b32_e32 v14, 16, v38
	v_and_b32_e32 v15, 0xffff0000, v38
	v_mul_f32_e32 v14, v1, v14
	v_mul_f32_e32 v15, v1, v15
	s_nop 0
	v_mul_f32_e32 v14, v44, v14
	v_mul_f32_e32 v15, v45, v15
	v_cvt_pk_bf16_f32 v14, v14, v15
	v_lshlrev_b32_e32 v15, 16, v39
	v_mul_f32_e32 v15, v1, v15
	v_mul_f32_e32 v15, v46, v15
	v_mul_f32_e32 v16, v47, v16
	v_cvt_pk_bf16_f32 v15, v15, v16
	global_store_dwordx4 v[10:11], v[12:15], off offset:640
	s_nop 0
	v_and_b32_e32 v16, 0xffff0000, v65
	v_mul_f32_e32 v16, v1, v16
	v_lshlrev_b32_e32 v12, 16, v62
	v_and_b32_e32 v13, 0xffff0000, v62
	v_mul_f32_e32 v12, v1, v12
	v_mul_f32_e32 v13, v1, v13
	v_mul_f32_e32 v12, v48, v12
	v_mul_f32_e32 v13, v49, v13
	v_cvt_pk_bf16_f32 v12, v12, v13
	v_lshlrev_b32_e32 v13, 16, v63
	v_and_b32_e32 v14, 0xffff0000, v63
	v_mul_f32_e32 v13, v1, v13
	v_mul_f32_e32 v14, v1, v14
	v_mul_f32_e32 v13, v50, v13
	v_mul_f32_e32 v14, v51, v14
	v_cvt_pk_bf16_f32 v13, v13, v14
	v_lshlrev_b32_e32 v14, 16, v64
	v_and_b32_e32 v15, 0xffff0000, v64
	v_mul_f32_e32 v14, v1, v14
	v_mul_f32_e32 v15, v1, v15
	v_mul_f32_e32 v14, v58, v14
	v_mul_f32_e32 v15, v59, v15
	v_cvt_pk_bf16_f32 v14, v14, v15
	v_lshlrev_b32_e32 v15, 16, v65
	v_mul_f32_e32 v15, v1, v15
	v_mul_f32_e32 v15, v60, v15
	v_mul_f32_e32 v16, v61, v16
	v_cvt_pk_bf16_f32 v15, v15, v16
	global_store_dwordx4 v[10:11], v[12:15], off offset:704
	s_nop 0
	v_and_b32_e32 v16, 0xffff0000, v85
	v_mul_f32_e32 v16, v1, v16
	v_lshlrev_b32_e32 v12, 16, v82
	v_and_b32_e32 v13, 0xffff0000, v82
	v_mul_f32_e32 v12, v1, v12
	v_mul_f32_e32 v13, v1, v13
	v_mul_f32_e32 v12, v66, v12
	v_mul_f32_e32 v13, v67, v13
	v_cvt_pk_bf16_f32 v12, v12, v13
	v_lshlrev_b32_e32 v13, 16, v83
	v_and_b32_e32 v14, 0xffff0000, v83
	v_mul_f32_e32 v13, v1, v13
	v_mul_f32_e32 v14, v1, v14
	v_mul_f32_e32 v13, v68, v13
	v_mul_f32_e32 v14, v69, v14
	v_cvt_pk_bf16_f32 v13, v13, v14
	v_lshlrev_b32_e32 v14, 16, v84
	v_and_b32_e32 v15, 0xffff0000, v84
	v_mul_f32_e32 v14, v1, v14
	v_mul_f32_e32 v15, v1, v15
	v_mul_f32_e32 v14, v70, v14
	v_mul_f32_e32 v15, v71, v15
	v_cvt_pk_bf16_f32 v14, v14, v15
	v_lshlrev_b32_e32 v15, 16, v85
	v_mul_f32_e32 v15, v1, v15
	v_mul_f32_e32 v15, v72, v15
	v_mul_f32_e32 v16, v73, v16
	v_cvt_pk_bf16_f32 v15, v15, v16
	global_store_dwordx4 v[10:11], v[12:15], off offset:768
	s_nop 0
	v_and_b32_e32 v16, 0xffff0000, v89
	v_mul_f32_e32 v16, v1, v16
	v_lshlrev_b32_e32 v12, 16, v86
	v_and_b32_e32 v13, 0xffff0000, v86
	v_mul_f32_e32 v12, v1, v12
	v_mul_f32_e32 v13, v1, v13
	v_mul_f32_e32 v12, v74, v12
	v_mul_f32_e32 v13, v75, v13
	v_cvt_pk_bf16_f32 v12, v12, v13
	v_lshlrev_b32_e32 v13, 16, v87
	v_and_b32_e32 v14, 0xffff0000, v87
	v_mul_f32_e32 v13, v1, v13
	v_mul_f32_e32 v14, v1, v14
	v_mul_f32_e32 v13, v76, v13
	v_mul_f32_e32 v14, v77, v14
	v_cvt_pk_bf16_f32 v13, v13, v14
	v_lshlrev_b32_e32 v14, 16, v88
	v_and_b32_e32 v15, 0xffff0000, v88
	v_mul_f32_e32 v14, v1, v14
	v_mul_f32_e32 v15, v1, v15
	v_mul_f32_e32 v14, v78, v14
	v_mul_f32_e32 v15, v79, v15
	v_cvt_pk_bf16_f32 v14, v14, v15
	v_lshlrev_b32_e32 v15, 16, v89
	v_mul_f32_e32 v15, v1, v15
	v_mul_f32_e32 v15, v80, v15
	v_mul_f32_e32 v16, v81, v16
	v_cvt_pk_bf16_f32 v15, v15, v16
	global_store_dwordx4 v[10:11], v[12:15], off offset:832
	s_nop 0
	v_and_b32_e32 v16, 0xffff0000, v55
	v_mul_f32_e32 v16, v1, v16
	v_lshlrev_b32_e32 v12, 16, v52
	v_and_b32_e32 v13, 0xffff0000, v52
	v_mul_f32_e32 v12, v1, v12
	v_mul_f32_e32 v13, v1, v13
	v_mul_f32_e32 v12, v90, v12
	v_mul_f32_e32 v13, v91, v13
	v_cvt_pk_bf16_f32 v12, v12, v13
	v_lshlrev_b32_e32 v13, 16, v53
	v_and_b32_e32 v14, 0xffff0000, v53
	v_mul_f32_e32 v13, v1, v13
	v_mul_f32_e32 v14, v1, v14
	v_mul_f32_e32 v13, v92, v13
	v_mul_f32_e32 v14, v93, v14
	v_cvt_pk_bf16_f32 v13, v13, v14
	v_lshlrev_b32_e32 v14, 16, v54
	v_and_b32_e32 v15, 0xffff0000, v54
	v_mul_f32_e32 v14, v1, v14
	v_mul_f32_e32 v15, v1, v15
	v_mul_f32_e32 v14, v94, v14
	v_mul_f32_e32 v15, v95, v15
	v_cvt_pk_bf16_f32 v14, v14, v15
	v_lshlrev_b32_e32 v15, 16, v55
	v_mul_f32_e32 v15, v1, v15
	v_mul_f32_e32 v15, v96, v15
	v_mul_f32_e32 v16, v97, v16
	v_cvt_pk_bf16_f32 v15, v15, v16
	global_store_dwordx4 v[10:11], v[12:15], off offset:896
	s_nop 0
	s_nop 0
	v_lshlrev_b32_e32 v12, 16, v6
	v_and_b32_e32 v6, 0xffff0000, v6
	v_mul_f32_e32 v12, v1, v12
	v_mul_f32_e32 v6, v1, v6
	v_mul_f32_e32 v12, v98, v12
	v_mul_f32_e32 v6, v99, v6
	v_cvt_pk_bf16_f32 v6, v12, v6
	v_lshlrev_b32_e32 v12, 16, v7
	v_and_b32_e32 v7, 0xffff0000, v7
	v_mul_f32_e32 v12, v1, v12
	v_mul_f32_e32 v7, v1, v7
	v_mul_f32_e32 v12, v100, v12
	v_mul_f32_e32 v7, v101, v7
	v_cvt_pk_bf16_f32 v7, v12, v7
	v_lshlrev_b32_e32 v12, 16, v8
	v_and_b32_e32 v8, 0xffff0000, v8
	v_mul_f32_e32 v12, v1, v12
	v_mul_f32_e32 v8, v1, v8
	v_mul_f32_e32 v2, v2, v12
	v_mul_f32_e32 v3, v3, v8
	v_cvt_pk_bf16_f32 v8, v2, v3
	v_lshlrev_b32_e32 v2, 16, v9
	v_and_b32_e32 v3, 0xffff0000, v9
	v_mul_f32_e32 v2, v1, v2
	v_mul_f32_e32 v1, v1, v3
	v_mul_f32_e32 v2, v4, v2
	v_mul_f32_e32 v1, v5, v1
	v_cvt_pk_bf16_f32 v9, v2, v1
	global_store_dwordx4 v[10:11], v[6:9], off offset:960
	s_cbranch_scc0 .LBB0_599

.LBB0_563:
	s_lshr_b32 s0, s49, 3
	s_and_b32 s6, s0, 63
	v_readlane_b32 s0, v255, 55
	s_and_b32 s0, s0, 7
	v_readlane_b32 s56, v253, 18
	v_lshl_or_b32 v2, s0, 9, v165
	v_readlane_b32 s8, v255, 53
	v_lshlrev_b32_e32 v160, 1, v2
	v_lshlrev_b32_e32 v12, 2, v2
	v_mov_b32_e32 v13, v161
	v_readlane_b32 s66, v253, 28
	v_readlane_b32 s67, v253, 29
	v_readlane_b32 s9, v255, 54
	v_cndmask_b32_e64 v2, v1, 0, s[80:81]
	v_lshl_add_u64 v[110:111], s[66:67], 0, v[12:13]
	v_lshl_add_u64 v[112:113], s[8:9], 0, v[12:13]
	s_cmp_eq_u32 s98, 0
	s_cbranch_scc1 .Lp5_wl_f1
	v_lshrrev_b32_e32 v128, 5, v0
	v_and_b32_e32 v129, 7, v128
	v_lshrrev_b32_e32 v128, 3, v128
	v_lshlrev_b32_e32 v130, 8, v129
	v_mul_u32_u24_e32 v132, 0x12000, v128
	v_add_u32_e32 v132, v132, v130
	v_mov_b32_e32 v133, 0
	v_mov_b32_e32 v137, 0
	v_lshl_add_u64 v[134:135], v[110:111], 0, v[132:133]
	global_load_dwordx2 v[144:145], v[134:135], off
	v_sub_u32_e32 v131, 1, v128
	v_mul_u32_u24_e32 v136, 0xc000, v131
	v_lshl_add_u64 v[134:135], v[134:135], 0, v[136:137]
	global_load_dwordx2 v[146:147], v[134:135], off
	v_cmp_eq_u32_e64 s[72:73], 1, v128
	v_mul_u32_u24_e32 v136, 0x6000, v131
	v_add_u32_e32 v136, v136, v130
	v_lshlrev_b32_e32 v138, 8, v128
	v_sub_u32_e32 v136, v136, v138
	v_ashrrev_i32_e32 v137, 31, v136
	v_cndmask_b32_e64 v134, v110, v112, s[72:73]
	v_cndmask_b32_e64 v135, v111, v113, s[72:73]
	v_lshl_add_u64 v[134:135], v[134:135], 0, v[136:137]
	global_load_dwordx2 v[148:149], v[134:135], off
	v_and_b32_e32 v138, 31, v0
	v_lshlrev_b32_e32 v138, 3, v138
	v_mul_u32_u24_e32 v139, 0x500, v129
	v_add_u32_e32 v138, v138, v139
	v_add_u32_e32 v138, 0x24000, v138
	v_mul_u32_u24_e32 v139, 0x300, v128
	v_add_u32_e32 v150, v138, v139
	v_lshl_add_u32 v151, v128, 8, v138
	v_readlane_b32 s74, v253, 38
	v_readlane_b32 s75, v253, 39
	v_readlane_b32 s76, v255, 58
	s_lshl_b32 s76, s76, 2
	s_add_u32 s74, s74, s76
	s_addc_u32 s75, s75, 0
	v_and_b32_e32 v143, 0x7f, v0
	v_lshlrev_b32_e32 v143, 4, v143
	v_add_u32_e32 v156, 0x26800, v143
	global_load_dwordx4 v[152:155], v143, s[74:75]
.Lp5_wl_f1:
	v_cndmask_b32_e64 v1, v205, 0, s[80:81]
	v_cndmask_b32_e64 v12, v206, 0, s[80:81]
	v_lshlrev_b32_e32 v13, 16, v2
	v_fma_f32 v13, v176, v13, v184
	v_and_b32_e32 v70, 0xffff0000, v2
	v_lshlrev_b32_e32 v81, 16, v1
	v_lshlrev_b32_e32 v85, 16, v12
	v_lshlrev_b32_e32 v84, 16, v3
	v_mov_b32_e32 v74, v182
	v_mov_b32_e32 v75, v180
	v_fma_f32 v80, v177, v70, v185
	v_fmac_f32_e32 v13, v178, v81
	v_pk_mul_f32 v[70:71], v[74:75], v[84:85]
	v_and_b32_e32 v83, 0xffff0000, v1
	v_add_f32_e32 v13, v71, v13
	v_add_f32_e32 v13, v70, v13
	v_mul_f32_e32 v70, 0xbfb8aa3b, v13
	v_exp_f32_e32 v82, v70
	v_and_b32_e32 v91, 0xffff0000, v12
	v_and_b32_e32 v90, 0xffff0000, v3
	v_mov_b32_e32 v92, v183
	v_add_f32_e32 v82, 1.0, v82
	v_rcp_f32_e32 v82, v82
	v_mov_b32_e32 v93, v181
	v_fmac_f32_e32 v80, v179, v83
	v_pk_mul_f32 v[94:95], v[92:93], v[90:91]
	v_mul_f32_e32 v13, v13, v82
	v_add_f32_e32 v80, v95, v80
	v_add_f32_e32 v82, v94, v80
	v_mul_f32_e32 v80, 0xbfb8aa3b, v82
	v_exp_f32_e32 v80, v80
	ds_read_b128 v[76:79], v242
	ds_read_b128 v[70:73], v242 offset:16
	v_mov_b32_e32 v94, v178
	v_mov_b32_e32 v95, v176
	v_add_f32_e32 v80, 1.0, v80
	v_rcp_f32_e32 v98, v80
	v_mov_b32_e32 v80, v85
	v_lshlrev_b32_e32 v87, 16, v4
	v_lshlrev_b32_e32 v86, 16, v5
	v_pk_mul_f32 v[80:81], v[94:95], v[80:81]
	v_mul_f32_e32 v82, v82, v98
	s_waitcnt lgkmcnt(1)
	v_mul_f32_e32 v13, v13, v76
	v_pk_mul_f32 v[96:97], v[94:95], v[84:85]
	v_mul_f32_e32 v106, v82, v76
	v_pk_mov_b32 v[84:85], v[86:87], v[84:85] op_sel:[1,0]
	v_add_f32_e32 v76, v81, v184
	v_pk_mul_f32 v[104:105], v[74:75], v[84:85]
	v_add_f32_e32 v76, v80, v76
	v_add_f32_e32 v76, v105, v76
	v_add_f32_e32 v76, v104, v76
	v_mul_f32_e32 v80, 0xbfb8aa3b, v76
	v_add_f32_e32 v97, v97, v184
	v_exp_f32_e32 v104, v80
	v_pk_mul_f32 v[80:81], v[74:75], v[86:87]
	v_add_f32_e32 v96, v96, v97
	v_add_f32_e32 v81, v81, v96
	v_add_f32_e32 v96, v80, v81
	v_mul_f32_e32 v80, 0xbfb8aa3b, v96
	v_exp_f32_e32 v80, v80
	v_add_f32_e32 v97, 1.0, v104
	v_rcp_f32_e32 v97, v97
	v_mov_b32_e32 v98, v179
	v_add_f32_e32 v80, 1.0, v80
	v_rcp_f32_e32 v104, v80
	v_mov_b32_e32 v99, v177
	v_mov_b32_e32 v82, v91
	v_mul_f32_e32 v76, v76, v97
	v_and_b32_e32 v89, 0xffff0000, v4
	v_and_b32_e32 v88, 0xffff0000, v5
	v_pk_mul_f32 v[82:83], v[98:99], v[82:83]
	v_mul_f32_e32 v105, v76, v77
	v_mul_f32_e32 v76, v96, v104
	v_pk_mul_f32 v[100:101], v[98:99], v[90:91]
	v_mul_f32_e32 v104, v76, v78
	v_pk_mov_b32 v[90:91], v[88:89], v[90:91] op_sel:[1,0]
	v_add_f32_e32 v76, v83, v185
	v_pk_mul_f32 v[96:97], v[92:93], v[90:91]
	v_add_f32_e32 v76, v82, v76
	v_add_f32_e32 v76, v97, v76
	v_add_f32_e32 v76, v96, v76
	v_mul_f32_e32 v82, 0xbfb8aa3b, v76
	v_add_f32_e32 v97, v101, v185
	v_exp_f32_e32 v96, v82
	v_pk_mul_f32 v[82:83], v[92:93], v[88:89]
	v_add_f32_e32 v97, v100, v97
	v_add_f32_e32 v83, v83, v97
	v_add_f32_e32 v97, v82, v83
	v_mul_f32_e32 v82, 0xbfb8aa3b, v97
	v_exp_f32_e32 v100, v82
	v_pk_mul_f32 v[82:83], v[94:95], v[84:85]
	v_add_f32_e32 v84, 1.0, v96
	v_rcp_f32_e32 v96, v84
	v_add_f32_e32 v84, 1.0, v100
	v_rcp_f32_e32 v100, v84
	v_lshlrev_b32_e32 v103, 16, v6
	v_mul_f32_e32 v76, v76, v96
	v_lshlrev_b32_e32 v102, 16, v7
	v_mul_f32_e32 v107, v76, v77
	v_mul_f32_e32 v76, v97, v100
	v_pk_mul_f32 v[84:85], v[94:95], v[86:87]
	v_mul_f32_e32 v108, v76, v78
	v_pk_mov_b32 v[86:87], v[102:103], v[86:87] op_sel:[1,0]
	v_add_f32_e32 v78, v83, v184
	v_pk_mul_f32 v[100:101], v[74:75], v[86:87]
	v_add_f32_e32 v78, v82, v78
	v_add_f32_e32 v78, v101, v78
	v_add_f32_e32 v78, v100, v78
	v_mul_f32_e32 v82, 0xbfb8aa3b, v78
	v_add_f32_e32 v85, v85, v184
	v_exp_f32_e32 v100, v82
	v_pk_mul_f32 v[82:83], v[74:75], v[102:103]
	v_add_f32_e32 v84, v84, v85
	v_add_f32_e32 v83, v83, v84
	v_add_f32_e32 v84, v82, v83
	v_mul_f32_e32 v82, 0xbfb8aa3b, v84
	v_exp_f32_e32 v82, v82
	v_add_f32_e32 v85, 1.0, v100
	v_rcp_f32_e32 v85, v85
	v_and_b32_e32 v81, 0xffff0000, v6
	v_add_f32_e32 v82, 1.0, v82
	v_rcp_f32_e32 v100, v82
	v_and_b32_e32 v80, 0xffff0000, v7
	v_pk_mul_f32 v[76:77], v[98:99], v[90:91]
	v_mul_f32_e32 v78, v78, v85
	v_mul_f32_e32 v101, v78, v79
	v_mul_f32_e32 v78, v84, v100
	v_pk_mul_f32 v[84:85], v[94:95], v[86:87]
	v_pk_mov_b32 v[86:87], v[80:81], v[88:89] op_sel:[1,0]
	v_add_f32_e32 v77, v77, v185
	v_pk_mul_f32 v[90:91], v[98:99], v[88:89]
	v_pk_mul_f32 v[88:89], v[92:93], v[86:87]
	v_add_f32_e32 v76, v76, v77
	v_add_f32_e32 v76, v89, v76
	s_waitcnt lgkmcnt(0)
	v_mul_f32_e32 v100, v78, v70
	v_add_f32_e32 v78, v88, v76
	v_mul_f32_e32 v76, 0xbfb8aa3b, v78
	v_add_f32_e32 v89, v91, v185
	v_exp_f32_e32 v88, v76
	v_pk_mul_f32 v[76:77], v[92:93], v[80:81]
	v_add_f32_e32 v89, v90, v89
	v_add_f32_e32 v77, v77, v89
	v_add_f32_e32 v109, v76, v77
	v_mul_f32_e32 v76, 0xbfb8aa3b, v109
	v_exp_f32_e32 v89, v76
	v_add_f32_e32 v88, 1.0, v88
	v_lshlrev_b32_e32 v97, 16, v8
	v_lshlrev_b32_e32 v96, 16, v9
	v_rcp_f32_e32 v114, v88
	v_add_f32_e32 v88, 1.0, v89
	v_rcp_f32_e32 v115, v88
	v_pk_mov_b32 v[88:89], v[96:97], v[102:103] op_sel:[1,0]
	v_add_f32_e32 v85, v85, v184
	v_pk_mul_f32 v[90:91], v[74:75], v[88:89]
	v_add_f32_e32 v84, v84, v85
	v_add_f32_e32 v84, v91, v84
	v_add_f32_e32 v90, v90, v84
	v_mul_f32_e32 v84, 0xbfb8aa3b, v90
	v_exp_f32_e32 v84, v84
	v_mul_f32_e32 v78, v78, v114
	v_mul_f32_e32 v91, v78, v79
	v_mul_f32_e32 v78, v109, v115
	v_add_f32_e32 v79, 1.0, v84
	v_and_b32_e32 v83, 0xffff0000, v8
	v_and_b32_e32 v82, 0xffff0000, v9
	v_pk_mul_f32 v[76:77], v[94:95], v[102:103]
	v_rcp_f32_e32 v102, v79
	v_mul_f32_e32 v103, v78, v70
	v_pk_mul_f32 v[78:79], v[98:99], v[86:87]
	v_pk_mul_f32 v[84:85], v[98:99], v[80:81]
	v_pk_mov_b32 v[80:81], v[82:83], v[80:81] op_sel:[1,0]
	v_add_f32_e32 v79, v79, v185
	v_pk_mul_f32 v[86:87], v[92:93], v[80:81]
	v_add_f32_e32 v78, v78, v79
	v_add_f32_e32 v78, v87, v78
	v_add_f32_e32 v86, v86, v78
	v_mul_f32_e32 v78, 0xbfb8aa3b, v86
	v_exp_f32_e32 v87, v78
	v_mul_f32_e32 v70, v90, v102
	v_mul_f32_e32 v90, v70, v71
	v_add_f32_e32 v70, v77, v184
	v_add_f32_e32 v77, 1.0, v87
	v_rcp_f32_e32 v77, v77
	v_pk_mul_f32 v[78:79], v[74:75], v[96:97]
	v_add_f32_e32 v70, v76, v70
	v_add_f32_e32 v70, v79, v70
	v_add_f32_e32 v70, v78, v70
	v_mul_f32_e32 v78, v86, v77
	v_pk_mul_f32 v[76:77], v[92:93], v[82:83]
	v_mul_f32_e32 v83, 0xbfb8aa3b, v70
	v_exp_f32_e32 v83, v83
	v_add_f32_e32 v79, v85, v185
	v_add_f32_e32 v79, v84, v79
	v_add_f32_e32 v77, v77, v79
	v_add_f32_e32 v84, v76, v77
	v_add_f32_e32 v76, 1.0, v83
	v_rcp_f32_e32 v76, v76
	v_mul_f32_e32 v77, 0xbfb8aa3b, v84
	v_exp_f32_e32 v77, v77
	v_mul_f32_e32 v83, v78, v71
	v_mul_f32_e32 v70, v70, v76
	v_mul_f32_e32 v85, v70, v72
	v_add_f32_e32 v70, 1.0, v77
	v_rcp_f32_e32 v86, v70
	v_pk_mul_f32 v[70:71], v[94:95], v[88:89]
	v_lshlrev_b32_e32 v78, 16, v10
	v_mov_b32_e32 v79, v96
	v_add_f32_e32 v71, v71, v184
	v_pk_mul_f32 v[74:75], v[74:75], v[78:79]
	v_add_f32_e32 v70, v70, v71
	v_pk_mul_f32 v[76:77], v[98:99], v[80:81]
	v_add_f32_e32 v70, v75, v70
	v_add_f32_e32 v74, v74, v70
	v_and_b32_e32 v70, 0xffff0000, v10
	v_mov_b32_e32 v71, v82
	v_add_f32_e32 v75, v77, v185
	v_pk_mul_f32 v[70:71], v[92:93], v[70:71]
	v_add_f32_e32 v75, v76, v75
	v_add_f32_e32 v71, v71, v75
	v_add_f32_e32 v70, v70, v71
	v_mul_f32_e32 v75, 0xbfb8aa3b, v70
	v_mul_f32_e32 v71, 0xbfb8aa3b, v74
	v_exp_f32_e32 v75, v75
	v_exp_f32_e32 v71, v71
	s_lshl_b32 s1, s6, 7
	s_add_i32 s6, s5, s6
	v_add_f32_e32 v75, 1.0, v75
	v_add_f32_e32 v71, 1.0, v71
	v_rcp_f32_e32 v75, v75
	v_rcp_f32_e32 v71, v71
	s_ashr_i32 s7, s6, 31
	s_lshl_b64 s[6:7], s[6:7], 20
	v_mul_f32_e32 v70, v70, v75
	v_mul_f32_e32 v76, v84, v86
	v_mul_f32_e32 v71, v74, v71
	v_mul_f32_e32 v78, v70, v73
	v_cvt_pk_bf16_f32 v70, v13, v105
	v_or_b32_e32 v13, s6, v170
	s_add_i32 s1, s1, s4
	v_mul_f32_e32 v77, v76, v72
	v_mul_f32_e32 v74, v71, v73
	v_cvt_pk_bf16_f32 v71, v104, v101
	v_cvt_pk_bf16_f32 v72, v100, v90
	v_cvt_pk_bf16_f32 v73, v85, v74
	v_lshl_or_b32 v114, s0, 17, v13
	v_add_u32_e32 v13, s1, v211
	v_cvt_pk_bf16_f32 v74, v106, v107
	v_cvt_pk_bf16_f32 v75, v108, v91
	v_cvt_pk_bf16_f32 v76, v103, v83
	v_cvt_pk_bf16_f32 v77, v77, v78
	ds_write_b128 v227, v[70:73]
	ds_write_b128 v227, v[74:77] offset:272
	ds_write_b128 v229, v[14:17]
	ds_write_b128 v231, v[18:21]
	v_mad_i64_i32 v[70:71], s[4:5], v13, s11, v[160:161]
	v_add_u32_e32 v13, s1, v171
	v_mov_b32_e32 v115, s7
	s_mov_b64 s[6:7], 0x45c00080
	v_mad_i64_i32 v[118:119], s[4:5], v13, s11, v[160:161]
	v_add_u32_e32 v13, s1, v204
	v_lshl_add_u64 v[116:117], v[70:71], 0, s[6:7]
	v_mad_i64_i32 v[70:71], s[4:5], v13, s11, v[160:161]
	v_add_u32_e32 v13, s1, v163
	v_lshl_add_u64 v[120:121], v[70:71], 0, s[6:7]
	v_mad_i64_i32 v[70:71], s[4:5], v13, s11, v[160:161]
	v_add_u32_e32 v13, s1, v173
	v_lshl_add_u64 v[122:123], v[70:71], 0, s[6:7]
	v_mad_i64_i32 v[70:71], s[4:5], v13, s11, v[160:161]
	v_lshl_add_u64 v[124:125], v[70:71], 0, s[6:7]
	v_add_u32_e32 v70, s1, v232
	v_ashrrev_i32_e32 v71, 31, v70
	v_lshlrev_b64 v[126:127], 13, v[70:71]
	v_or_b32_e32 v13, v162, v126
	s_mov_b32 s2, 0
	v_lshl_or_b32 v126, s0, 10, v13
	v_lshl_add_u64 v[198:199], s[92:93], 0, v[126:127]
	v_add_co_u32_e32 v198, vcc, 0x3dc00000, v198
	s_nop 1
	v_addc_co_u32_e32 v199, vcc, 0, v199, vcc
	global_load_dwordx4 v[74:77], v[198:199], off
	global_load_dwordx4 v[70:73], v[198:199], off offset:64
	v_mov_b32_e32 v140, 0
	s_mov_b64 s[0:1], 0
	v_mov_b32_e32 v13, v245
	v_mov_b32_e32 v141, v244
	v_mov_b32_e32 v142, v243
	v_readlane_b32 s57, v253, 19
	v_readlane_b32 s58, v253, 20
	v_readlane_b32 s59, v253, 21
	v_readlane_b32 s60, v253, 22
	v_readlane_b32 s61, v253, 23
	v_readlane_b32 s62, v253, 24
	v_readlane_b32 s63, v253, 25
	v_readlane_b32 s64, v253, 26
	v_readlane_b32 s65, v253, 27
	v_readlane_b32 s68, v253, 30
	v_readlane_b32 s69, v253, 31
	v_readlane_b32 s70, v253, 32
	v_readlane_b32 s71, v253, 33
	s_cmp_eq_u32 s98, 0
	s_cbranch_scc1 .Lp5_wl_f2
	s_waitcnt vmcnt(2)
	ds_write_b64 v150, v[144:145]
	ds_write_b64 v150, v[148:149] offset:256
	ds_write_b64 v151, v[146:147] offset:512
	ds_write_b128 v156, v[152:155]
	s_mov_b32 s98, 0
.Lp5_wl_f2:
	s_waitcnt lgkmcnt(0)
	s_barrier
	s_branch .LBB0_565

.Lp5_z0skip:
	global_load_dwordx4 v[200:203], v[198:199], off offset:128
	global_load_dwordx4 v[216:219], v[198:199], off offset:192
	s_cmpk_eq_i32 s0, 0x700
	s_cbranch_scc1 .Lp5_pf_skip
	global_load_dword v2, v124, s[92:93]
	global_load_dword v1, v122, s[92:93]
	global_load_dword v12, v120, s[92:93]
	s_add_u32 s4, s92, 0x45c00000
	s_addc_u32 s5, s93, 0
	global_load_dword v3, v118, s[4:5] offset:128
	s_add_u32 s4, s4, 0x3000
	s_addc_u32 s5, s5, 0
	global_load_dword v4, v118, s[4:5] offset:128
	s_add_u32 s4, s4, 0x3000
	s_addc_u32 s5, s5, 0
	global_load_dword v5, v118, s[4:5] offset:128
	s_add_u32 s4, s4, 0x3000
	s_addc_u32 s5, s5, 0
	global_load_dword v6, v118, s[4:5] offset:128
	s_add_u32 s4, s4, 0x3000
	s_addc_u32 s5, s5, 0
	global_load_dword v7, v118, s[4:5] offset:128
	s_add_u32 s4, s4, 0x3000
	s_addc_u32 s5, s5, 0
	global_load_dword v8, v118, s[4:5] offset:128
	s_add_u32 s4, s4, 0x3000
	s_addc_u32 s5, s5, 0
	global_load_dword v9, v118, s[4:5] offset:128
	global_load_dword v10, v116, s[92:93]
	s_mov_b32 s5, 0
	v_lshl_add_u64 v[94:95], s[92:93], 0, v[114:115]
	s_mov_b32 s4, 0x5e004000
	v_lshl_add_u64 v[16:17], v[94:95], 0, s[4:5]
	global_load_dwordx4 v[14:17], v[16:17], off
	s_mov_b32 s4, 0x5e006000
	v_lshl_add_u64 v[18:19], v[94:95], 0, s[4:5]
	global_load_dwordx4 v[18:21], v[18:19], off

.LBB0_573:
.LBB0_574:
	s_and_b64 s[6:7], s[90:91], exec
	s_mov_b32 s6, 0xec00
	s_cselect_b32 s6, 0x17400, s6
	s_add_i32 s6, s6, 0
	v_add3_u32 v130, s6, v162, v222
	ds_read_b128 v[94:97], v130
	ds_read_b128 v[98:101], v130 offset:64
	ds_read_b128 v[102:105], v130 offset:4352
	ds_read_b128 v[106:109], v130 offset:4416
	ds_read_b128 v[132:135], v130 offset:8704
	ds_read_b128 v[136:139], v130 offset:8768
	ds_read_b128 v[144:147], v130 offset:13056
	ds_read_b128 v[148:151], v130 offset:13120
	s_waitcnt lgkmcnt(7)
	v_mfma_f32_16x16x32_bf16 v[94:97], v[94:97], v[22:25], 0
	s_waitcnt lgkmcnt(5)
	v_mfma_f32_16x16x32_bf16 v[102:105], v[102:105], v[22:25], 0
	s_waitcnt lgkmcnt(3)
	v_mfma_f32_16x16x32_bf16 v[132:135], v[132:135], v[22:25], 0
	s_waitcnt lgkmcnt(1)
	v_mfma_f32_16x16x32_bf16 v[144:147], v[144:147], v[22:25], 0
	ds_read_b128 v[152:155], v130 offset:128
	ds_read_b128 v[186:189], v130 offset:4480
	ds_read_b128 v[190:193], v130 offset:8832
	ds_read_b128 v[194:197], v130 offset:13184
	v_mfma_f32_16x16x32_bf16 v[94:97], v[98:101], v[26:29], v[94:97]
	v_mfma_f32_16x16x32_bf16 v[98:101], v[106:109], v[26:29], v[102:105]
	s_waitcnt lgkmcnt(4)
	v_mfma_f32_16x16x32_bf16 v[106:109], v[148:151], v[26:29], v[144:147]
	v_mfma_f32_16x16x32_bf16 v[102:105], v[136:139], v[26:29], v[132:135]
	s_nop 2
	ds_read_b128 v[132:135], v130 offset:192
	ds_read_b128 v[136:139], v130 offset:4544
	ds_read_b128 v[144:147], v130 offset:8896
	ds_read_b128 v[148:151], v130 offset:13248
	s_waitcnt lgkmcnt(7)
	v_mfma_f32_16x16x32_bf16 v[94:97], v[152:155], v[30:33], v[94:97]
	s_waitcnt lgkmcnt(6)
	v_mfma_f32_16x16x32_bf16 v[98:101], v[186:189], v[30:33], v[98:101]
	s_waitcnt lgkmcnt(4)
	v_mfma_f32_16x16x32_bf16 v[106:109], v[194:197], v[30:33], v[106:109]
	v_mfma_f32_16x16x32_bf16 v[152:155], v[190:193], v[30:33], v[102:105]
	s_waitcnt lgkmcnt(3)
	v_mfma_f32_16x16x32_bf16 v[132:135], v[132:135], v[34:37], v[94:97]
	s_waitcnt lgkmcnt(2)
	v_mfma_f32_16x16x32_bf16 v[102:105], v[136:139], v[34:37], v[98:101]
	s_waitcnt lgkmcnt(1)
	v_mfma_f32_16x16x32_bf16 v[98:101], v[144:147], v[34:37], v[152:155]
	s_waitcnt lgkmcnt(0)
	v_mfma_f32_16x16x32_bf16 v[94:97], v[148:151], v[34:37], v[106:109]
	s_nop 2
	v_mul_f32_e32 v106, 0x3fb8aa3b, v131
	s_cmpk_eq_i32 s0, 0x700
	s_cbranch_scc1 .Lp5_zw_last
	s_waitcnt vmcnt(15)
	s_branch .Lp5_zw_done

.Lp5_cwd:
	v_cndmask_b32_e64 v2, v2, 0, s[80:81]
	v_cndmask_b32_e64 v1, v1, 0, s[80:81]
	v_cndmask_b32_e64 v12, v12, 0, s[80:81]
	s_add_i32 s4, s2, 1
	s_mul_i32 s4, s4, 0x500
	s_add_i32 s4, s4, 0x24000
	v_and_b32_e32 v100, 31, v0
	v_lshlrev_b32_e32 v100, 3, v100
	v_add_u32_e32 v100, s4, v100
	ds_read_b64 v[176:177], v100
	ds_read_b64 v[178:179], v100 offset:256
	ds_read_b64 v[180:181], v100 offset:512
	ds_read_b64 v[182:183], v100 offset:768
	ds_read_b64 v[184:185], v100 offset:1024
	ds_read_b128 v[96:99], v142
	ds_read_b128 v[70:73], v142 offset:16
	v_lshlrev_b32_e32 v100, 16, v2
	v_and_b32_e32 v128, 0xffff0000, v2
	v_lshlrev_b32_e32 v101, 16, v1
	v_and_b32_e32 v129, 0xffff0000, v1
	v_lshlrev_b32_e32 v102, 16, v12
	v_and_b32_e32 v130, 0xffff0000, v12
	v_lshlrev_b32_e32 v103, 16, v3
	v_and_b32_e32 v131, 0xffff0000, v3
	v_lshlrev_b32_e32 v104, 16, v4
	v_and_b32_e32 v132, 0xffff0000, v4
	v_lshlrev_b32_e32 v105, 16, v5
	v_and_b32_e32 v133, 0xffff0000, v5
	v_lshlrev_b32_e32 v106, 16, v6
	v_and_b32_e32 v134, 0xffff0000, v6
	v_lshlrev_b32_e32 v107, 16, v7
	v_and_b32_e32 v135, 0xffff0000, v7
	v_lshlrev_b32_e32 v108, 16, v8
	v_and_b32_e32 v136, 0xffff0000, v8
	v_lshlrev_b32_e32 v109, 16, v9
	v_and_b32_e32 v137, 0xffff0000, v9
	v_lshlrev_b32_e32 v95, 16, v10
	v_and_b32_e32 v138, 0xffff0000, v10
	s_waitcnt lgkmcnt(2)
	v_fma_f32 v148, v176, v100, v184
	v_fma_f32 v149, v177, v128, v185
	v_fmac_f32_e32 v148, v178, v101
	v_fmac_f32_e32 v149, v179, v129
	v_fmac_f32_e32 v148, v180, v102
	v_fmac_f32_e32 v149, v181, v130
	v_fmac_f32_e32 v148, v182, v103
	v_fmac_f32_e32 v149, v183, v131
	v_mul_f32_e32 v150, 0xbfb8aa3b, v148
	v_mul_f32_e32 v151, 0xbfb8aa3b, v149
	v_exp_f32_e32 v150, v150
	v_exp_f32_e32 v151, v151
	v_add_f32_e32 v150, 1.0, v150
	v_add_f32_e32 v151, 1.0, v151
	v_rcp_f32_e32 v150, v150
	v_rcp_f32_e32 v151, v151
	s_waitcnt lgkmcnt(0)
	v_mul_f32_e32 v148, v148, v150
	v_mul_f32_e32 v149, v149, v151
	v_mul_f32_e32 v100, v148, v96
	v_mul_f32_e32 v128, v149, v96
	v_fma_f32 v148, v176, v101, v184
	v_fma_f32 v149, v177, v129, v185
	v_fmac_f32_e32 v148, v178, v102
	v_fmac_f32_e32 v149, v179, v130
	v_fmac_f32_e32 v148, v180, v103
	v_fmac_f32_e32 v149, v181, v131
	v_fmac_f32_e32 v148, v182, v104
	v_fmac_f32_e32 v149, v183, v132
	v_mul_f32_e32 v150, 0xbfb8aa3b, v148
	v_mul_f32_e32 v151, 0xbfb8aa3b, v149
	v_exp_f32_e32 v150, v150
	v_exp_f32_e32 v151, v151
	v_add_f32_e32 v150, 1.0, v150
	v_add_f32_e32 v151, 1.0, v151
	v_rcp_f32_e32 v150, v150
	v_rcp_f32_e32 v151, v151
	v_mul_f32_e32 v148, v148, v150
	v_mul_f32_e32 v149, v149, v151
	v_mul_f32_e32 v101, v148, v97
	v_mul_f32_e32 v129, v149, v97
	v_fma_f32 v148, v176, v102, v184
	v_fma_f32 v149, v177, v130, v185
	v_fmac_f32_e32 v148, v178, v103
	v_fmac_f32_e32 v149, v179, v131
	v_fmac_f32_e32 v148, v180, v104
	v_fmac_f32_e32 v149, v181, v132
	v_fmac_f32_e32 v148, v182, v105
	v_fmac_f32_e32 v149, v183, v133
	v_mul_f32_e32 v150, 0xbfb8aa3b, v148
	v_mul_f32_e32 v151, 0xbfb8aa3b, v149
	v_exp_f32_e32 v150, v150
	v_exp_f32_e32 v151, v151
	v_add_f32_e32 v150, 1.0, v150
	v_add_f32_e32 v151, 1.0, v151
	v_rcp_f32_e32 v150, v150
	v_rcp_f32_e32 v151, v151
	v_mul_f32_e32 v148, v148, v150
	v_mul_f32_e32 v149, v149, v151
	v_mul_f32_e32 v102, v148, v98
	v_mul_f32_e32 v130, v149, v98
	v_fma_f32 v148, v176, v103, v184
	v_fma_f32 v149, v177, v131, v185
	v_fmac_f32_e32 v148, v178, v104
	v_fmac_f32_e32 v149, v179, v132
	v_fmac_f32_e32 v148, v180, v105
	v_fmac_f32_e32 v149, v181, v133
	v_fmac_f32_e32 v148, v182, v106
	v_fmac_f32_e32 v149, v183, v134
	v_mul_f32_e32 v150, 0xbfb8aa3b, v148
	v_mul_f32_e32 v151, 0xbfb8aa3b, v149
	v_exp_f32_e32 v150, v150
	v_exp_f32_e32 v151, v151
	v_add_f32_e32 v150, 1.0, v150
	v_add_f32_e32 v151, 1.0, v151
	v_rcp_f32_e32 v150, v150
	v_rcp_f32_e32 v151, v151
	v_mul_f32_e32 v148, v148, v150
	v_mul_f32_e32 v149, v149, v151
	v_mul_f32_e32 v103, v148, v99
	v_mul_f32_e32 v131, v149, v99
	v_fma_f32 v148, v176, v104, v184
	v_fma_f32 v149, v177, v132, v185
	v_fmac_f32_e32 v148, v178, v105
	v_fmac_f32_e32 v149, v179, v133
	v_fmac_f32_e32 v148, v180, v106
	v_fmac_f32_e32 v149, v181, v134
	v_fmac_f32_e32 v148, v182, v107
	v_fmac_f32_e32 v149, v183, v135
	v_mul_f32_e32 v150, 0xbfb8aa3b, v148
	v_mul_f32_e32 v151, 0xbfb8aa3b, v149
	v_exp_f32_e32 v150, v150
	v_exp_f32_e32 v151, v151
	v_add_f32_e32 v150, 1.0, v150
	v_add_f32_e32 v151, 1.0, v151
	v_rcp_f32_e32 v150, v150
	v_rcp_f32_e32 v151, v151
	v_mul_f32_e32 v148, v148, v150
	v_mul_f32_e32 v149, v149, v151
	v_mul_f32_e32 v104, v148, v70
	v_mul_f32_e32 v132, v149, v70
	v_fma_f32 v148, v176, v105, v184
	v_fma_f32 v149, v177, v133, v185
	v_fmac_f32_e32 v148, v178, v106
	v_fmac_f32_e32 v149, v179, v134
	v_fmac_f32_e32 v148, v180, v107
	v_fmac_f32_e32 v149, v181, v135
	v_fmac_f32_e32 v148, v182, v108
	v_fmac_f32_e32 v149, v183, v136
	v_mul_f32_e32 v150, 0xbfb8aa3b, v148
	v_mul_f32_e32 v151, 0xbfb8aa3b, v149
	v_exp_f32_e32 v150, v150
	v_exp_f32_e32 v151, v151
	v_add_f32_e32 v150, 1.0, v150
	v_add_f32_e32 v151, 1.0, v151
	v_rcp_f32_e32 v150, v150
	v_rcp_f32_e32 v151, v151
	v_mul_f32_e32 v148, v148, v150
	v_mul_f32_e32 v149, v149, v151
	v_mul_f32_e32 v105, v148, v71
	v_mul_f32_e32 v133, v149, v71
	v_fma_f32 v148, v176, v106, v184
	v_fma_f32 v149, v177, v134, v185
	v_fmac_f32_e32 v148, v178, v107
	v_fmac_f32_e32 v149, v179, v135
	v_fmac_f32_e32 v148, v180, v108
	v_fmac_f32_e32 v149, v181, v136
	v_fmac_f32_e32 v148, v182, v109
	v_fmac_f32_e32 v149, v183, v137
	v_mul_f32_e32 v150, 0xbfb8aa3b, v148
	v_mul_f32_e32 v151, 0xbfb8aa3b, v149
	v_exp_f32_e32 v150, v150
	v_exp_f32_e32 v151, v151
	v_add_f32_e32 v150, 1.0, v150
	v_add_f32_e32 v151, 1.0, v151
	v_rcp_f32_e32 v150, v150
	v_rcp_f32_e32 v151, v151
	v_mul_f32_e32 v148, v148, v150
	v_mul_f32_e32 v149, v149, v151
	v_mul_f32_e32 v106, v148, v72
	v_mul_f32_e32 v134, v149, v72
	v_fma_f32 v148, v176, v107, v184
	v_fma_f32 v149, v177, v135, v185
	v_fmac_f32_e32 v148, v178, v108
	v_fmac_f32_e32 v149, v179, v136
	v_fmac_f32_e32 v148, v180, v109
	v_fmac_f32_e32 v149, v181, v137
	v_fmac_f32_e32 v148, v182, v95
	v_fmac_f32_e32 v149, v183, v138
	v_mul_f32_e32 v150, 0xbfb8aa3b, v148
	v_mul_f32_e32 v151, 0xbfb8aa3b, v149
	v_exp_f32_e32 v150, v150
	v_exp_f32_e32 v151, v151
	v_add_f32_e32 v150, 1.0, v150
	v_add_f32_e32 v151, 1.0, v151
	v_rcp_f32_e32 v150, v150
	v_rcp_f32_e32 v151, v151
	v_mul_f32_e32 v148, v148, v150
	v_mul_f32_e32 v149, v149, v151
	v_mul_f32_e32 v107, v148, v73
	v_mul_f32_e32 v135, v149, v73
	s_and_b64 s[4:5], s[90:91], exec
	s_cselect_b32 s4, s51, s33
	s_add_i32 s6, 0, 0xec00
	v_cvt_pk_bf16_f32 v70, v100, v101
	v_cvt_pk_bf16_f32 v71, v102, v103
	v_cvt_pk_bf16_f32 v72, v104, v105
	v_cvt_pk_bf16_f32 v73, v106, v107
	v_cvt_pk_bf16_f32 v74, v128, v129
	v_cvt_pk_bf16_f32 v75, v130, v131
	v_cvt_pk_bf16_f32 v76, v132, v133
	v_cvt_pk_bf16_f32 v77, v134, v135
	v_add3_u32 v81, s4, v225, v226
	s_and_b64 s[4:5], s[90:91], exec
	s_cselect_b32 s4, s6, s10
	ds_write_b128 v81, v[70:73]
	ds_write_b128 v81, v[74:77] offset:272
	v_add3_u32 v70, s4, v228, v158
	ds_write_b128 v70, v[14:17]
	v_add3_u32 v70, s4, v230, v158
	ds_write_b128 v70, v[18:21]
	s_branch .LBB0_564

	.amdhsa_kernel _Z6mk_fwd4Args
		.amdhsa_group_segment_fixed_size 16384
		.amdhsa_private_segment_fixed_size 0
		.amdhsa_kernarg_size 456
		.amdhsa_user_sgpr_count 2
		.amdhsa_user_sgpr_dispatch_ptr 0
		.amdhsa_user_sgpr_queue_ptr 0
		.amdhsa_user_sgpr_kernarg_segment_ptr 1
		.amdhsa_user_sgpr_dispatch_id 0
		.amdhsa_user_sgpr_kernarg_preload_length 0
		.amdhsa_user_sgpr_kernarg_preload_offset 0
		.amdhsa_user_sgpr_private_segment_size 0
		.amdhsa_uses_dynamic_stack 0
		.amdhsa_enable_private_segment 0
		.amdhsa_system_sgpr_workgroup_id_x 1
		.amdhsa_system_sgpr_workgroup_id_y 0
		.amdhsa_system_sgpr_workgroup_id_z 0
		.amdhsa_system_sgpr_workgroup_info 0
		.amdhsa_system_vgpr_workitem_id 0
		.amdhsa_next_free_vgpr 256
		.amdhsa_next_free_sgpr 102
		.amdhsa_accum_offset 256
		.amdhsa_reserve_vcc 1
		.amdhsa_float_round_mode_32 0
		.amdhsa_float_round_mode_16_64 0
		.amdhsa_float_denorm_mode_32 3
		.amdhsa_float_denorm_mode_16_64 3
		.amdhsa_dx10_clamp 1
		.amdhsa_ieee_mode 1
		.amdhsa_fp16_overflow 0
		.amdhsa_tg_split 0
		.amdhsa_exception_fp_ieee_invalid_op 0
		.amdhsa_exception_fp_denorm_src 0
		.amdhsa_exception_fp_ieee_div_zero 0
		.amdhsa_exception_fp_ieee_overflow 0
		.amdhsa_exception_fp_ieee_underflow 0
		.amdhsa_exception_fp_ieee_inexact 0
		.amdhsa_exception_int_div_zero 0
	.end_amdhsa_kernel

amdhsa.kernels:
  - .agpr_count:     0
    .args:
      - .offset:         0
        .size:           200
        .value_kind:     by_value
      - .offset:         200
        .size:           4
        .value_kind:     hidden_block_count_x
      - .offset:         204
        .size:           4
        .value_kind:     hidden_block_count_y
      - .offset:         208
        .size:           4
        .value_kind:     hidden_block_count_z
      - .offset:         212
        .size:           2
        .value_kind:     hidden_group_size_x
      - .offset:         214
        .size:           2
        .value_kind:     hidden_group_size_y
      - .offset:         216
        .size:           2
        .value_kind:     hidden_group_size_z
      - .offset:         218
        .size:           2
        .value_kind:     hidden_remainder_x
      - .offset:         220
        .size:           2
        .value_kind:     hidden_remainder_y
      - .offset:         222
        .size:           2
        .value_kind:     hidden_remainder_z
      - .offset:         240
        .size:           8
        .value_kind:     hidden_global_offset_x
      - .offset:         248
        .size:           8
        .value_kind:     hidden_global_offset_y
      - .offset:         256
        .size:           8
        .value_kind:     hidden_global_offset_z
      - .offset:         264
        .size:           2
        .value_kind:     hidden_grid_dims
      - .offset:         320
        .size:           4
        .value_kind:     hidden_dynamic_lds_size
    .group_segment_fixed_size: 16384
    .kernarg_segment_align: 8
    .kernarg_segment_size: 456
    .language:       OpenCL C
    .language_version:
      - 2
      - 0
    .max_flat_workgroup_size: 512
    .name:           _Z6mk_fwd4Args
    .private_segment_fixed_size: 0
    .sgpr_count:     108
    .sgpr_spill_count: 188
    .symbol:         _Z6mk_fwd4Args.kd
    .uniform_work_group_size: 1
    .uses_dynamic_stack: false
    .vgpr_count:     256
    .vgpr_spill_count: 0
    .wavefront_size: 64
